# stack13 + P6 reuses the routing tables P5 left in LDS instead of reloading the counts and rebuilding them
# speedup vs baseline: 1.0004x; 1.0004x over previous
; #define LAS __attribute__((address_space(3)))
; __device__ __forceinline__ int fresh_lane() { unsigned z = 0u; asm volatile("" : "+v"(z)); return (int)__builtin_amdgcn_mbcnt_hi(~0u, __builtin_amdgcn_mbcnt_lo(~0u, z)); }
; __device__ __forceinline__ int moe_tables(const Ctx& c) {
;     LAS int* pstart = (LAS int*)(c.lds + TAB_PSTART); LAS int* cnts = (LAS int*)(c.lds + TAB_CNT); LAS unsigned char* pexp = (LAS unsigned char*)(c.lds + TAB_PEXP);
;     const int tid_ = c.wave * 64 + fresh_lane();
;     __syncthreads();
;     if (c.wave == 0) {
;         const int l_ = tid_; const int cc = l_ < NE ? (int)__hip_atomic_load(c.ctl + CW_COUNT + l_, RLX_AGENT) : 0; const int np = (cc + 255) >> 8; int inc = np;
; #pragma unroll
;         for (int o = 1; o < NE; o <<= 1) { const int t = __builtin_amdgcn_ds_bpermute(((l_ - o) & 63) << 2, inc); if (l_ >= o) inc += t; }
;         if (l_ < NE) { cnts[l_] = cc; pstart[l_] = inc - np; if (l_ == NE - 1) pstart[NE] = inc; } }
;     __syncthreads();
.LBB7_843:
	v_readlane_b32 s4, v254, 2
	v_readlane_b32 s5, v254, 3
	s_cmp_lt_i32 s4, 7
	s_cselect_b64 s[4:5], -1, 0
	s_and_b64 s[0:1], s[4:5], s[0:1]
	s_andn2_b64 vcc, exec, s[0:1]
	s_cbranch_vccnz .LBB7_928
	s_waitcnt vmcnt(0)
	v_mov_b32_e32 v0, 0
	v_readlane_b32 s0, v254, 5
	v_mbcnt_lo_u32_b32 v0, -1, v0
	v_mbcnt_hi_u32_b32 v3, -1, v0
	v_add_u32_e32 v0, s0, v3
	v_readlane_b32 s0, v254, 4
	v_mov_b32_e32 v1, 0
	s_cmp_gt_u32 s0, 63
	s_waitcnt lgkmcnt(0)
	s_barrier
	s_branch .LBB7_851
	v_cmp_gt_i32_e32 vcc, 32, v0
	s_and_saveexec_b64 s[0:1], vcc
	s_cbranch_execz .LBB7_847
	v_ashrrev_i32_e32 v1, 31, v0
	v_lshl_add_u64 v[4:5], v[0:1], 2, s[30:31]
	global_load_dword v1, v[4:5], off offset:256 sc1

; __device__ __forceinline__ int moe_tables(const Ctx& c) {
;     ...
;     const int npan = pstart[NE];
;     for (int pnl = tid_; pnl < npan; pnl += NWAVES * 64) { int e = 0;
; #pragma unroll
;         for (int st = 16; st >= 1; st >>= 1) if (pstart[e + st] <= pnl) e += st;
;         pexp[pnl] = (unsigned char)e; }
;     __syncthreads();
;     return __builtin_amdgcn_readfirstlane(npan);
.LBB7_851:
	s_add_i32 s0, 0, 0x20280
	v_mov_b32_e32 v1, s0
	s_waitcnt lgkmcnt(0)
	s_barrier
	ds_read_b32 v1, v1
	s_waitcnt lgkmcnt(0)
	s_mov_b64 vcc, 0
	s_and_saveexec_b64 s[0:1], vcc
	s_cbranch_execz .LBB7_854
	s_add_i32 s2, 0, 0x20240
	s_mov_b64 s[6:7], 0
	v_mov_b32_e32 v2, s2
	s_add_i32 s2, 0, 0x20200
